# attention item prologue: first key tile and output-gate loads issued with the query loads (one exposed round trip instead of two); plus permlane sums in the attention epilogue
# baseline (speedup 1.0000x reference)
; __device__ __forceinline__ float fexp2(float x) { return __builtin_amdgcn_exp2f(x); }
; __device__ __forceinline__ float siluf_(float x) { return x * __builtin_amdgcn_rcpf(1.f + fexp(-x)); }
; __device__ __forceinline__ float lo16(unsigned u) { return __uint_as_float(u << 16); }
; __device__ __forceinline__ float hi16(unsigned u) { return __uint_as_float(u & 0xffff0000u); }
; __device__ void phase_swa_mfma(const Params& p, int l, char* smem, int vb, int nvb, int pend, int oz) {
;     ...
;         const float snk = p.in[I_SINK][l * 4 + hq] * 1.4426950408889634f;
; #pragma unroll
;         for (int qt2 = 0; qt2 < 2; ++qt2) {
;             float ls = lsum[qt2];
;             ls += __shfl_xor(ls, 16);
;             ls += __shfl_xor(ls, 32);
;             const float mn = fmaxf(m[qt2], snk);
;             const float s1 = fexp2(m[qt2] - mn);
;             const float inv = s1 / (ls * s1 + fexp2(snk - mn));
;             const int tq = qt * 64 + 32 * qsub + 16 * qt2 + li;
;             bf16_t* zp = U + (qbase + tq) * LDU + C_SZ + hq * 64 + 4 * g;
; #pragma unroll
;             for (int dt = 0; dt < 4; ++dt) {
;                 const u32x2 zv = zpre[qt2][dt];
;                 u32x2 yv;
;                 yv[0] = cvt_pk(O[dt][qt2][0] * inv * siluf_(lo16(zv[0])), O[dt][qt2][1] * inv * siluf_(hi16(zv[0])));
;                 yv[1] = cvt_pk(O[dt][qt2][2] * inv * siluf_(lo16(zv[1])), O[dt][qt2][3] * inv * siluf_(hi16(zv[1])));
;                 *(u32x2*)(zp + 16 * dt) = yv;
.LBB0_178:
	s_add_i32 s2, s80, s56
	s_ashr_i32 s3, s2, 31
	v_readlane_b32 s4, v253, 18
	s_lshl_b64 s[2:3], s[2:3], 2
	v_readlane_b32 s16, v253, 30
	v_readlane_b32 s17, v253, 31
	s_add_u32 s2, s16, s2
	s_addc_u32 s3, s17, s3
	global_load_dword v21, v3, s[2:3]
	v_mov_b32_e32 v20, v131
	v_mov_b32_e32 v238, v131
	s_nop 1
	v_permlane16_swap_b32 v20, v238
	s_mov_b32 s4, 0x3fb8aa3b
	s_mov_b32 s21, s97
	s_add_i32 s53, s53, 1
	s_cmp_ge_i32 s53, s52
	s_waitcnt lgkmcnt(0)
	v_add_f32_e32 v20, v20, v238
	v_mov_b32_e32 v22, v20
	v_mov_b32_e32 v238, v20
	s_nop 1
	v_permlane32_swap_b32 v22, v238
	v_readlane_b32 s5, v253, 19
	v_readlane_b32 s6, v253, 20
	v_readlane_b32 s7, v253, 21
	v_readlane_b32 s8, v253, 22
	s_waitcnt lgkmcnt(0)
	v_add_f32_e32 v20, v22, v238
	v_max_f32_e32 v22, v127, v127
	v_readlane_b32 s9, v253, 23
	v_readlane_b32 s10, v253, 24
	v_readlane_b32 s11, v253, 25
	v_readlane_b32 s12, v253, 26
	v_readlane_b32 s13, v253, 27
	v_readlane_b32 s14, v253, 28
	v_readlane_b32 s15, v253, 29
	v_readlane_b32 s18, v253, 32
	v_readlane_b32 s19, v253, 33
	s_waitcnt vmcnt(0)
	v_mul_f32_e32 v30, 0x3fb8aa3b, v21
	v_max_f32_e32 v22, v22, v30
	v_sub_f32_e32 v23, v127, v22
	v_fma_f32 v22, v21, s4, -v22
	v_exp_f32_e32 v23, v23
	v_exp_f32_e32 v22, v22
	s_nop 0
	v_fmac_f32_e32 v22, v20, v23
	v_div_scale_f32 v20, s[2:3], v22, v22, v23
	v_rcp_f32_e32 v24, v20
	s_nop 0
	v_fma_f32 v25, -v20, v24, 1.0
	v_fmac_f32_e32 v24, v25, v24
	v_div_scale_f32 v25, vcc, v23, v22, v23
	v_mul_f32_e32 v26, v25, v24
	v_fma_f32 v27, -v20, v26, v25
	v_fmac_f32_e32 v26, v27, v24
	v_fma_f32 v20, -v20, v26, v25
	v_div_fmas_f32 v20, v20, v24, v26
	v_div_fixup_f32 v20, v20, v22, v23
	v_lshlrev_b32_e32 v22, 16, v128
	v_and_b32_e32 v23, 0xffff0000, v128
	v_mul_f32_e32 v24, 0xbfb8aa3b, v22
	v_mul_f32_e32 v25, 0xbfb8aa3b, v23
	v_exp_f32_e32 v24, v24
	v_exp_f32_e32 v25, v25
	v_pk_mul_f32 v[26:27], v[64:65], v[20:21] op_sel_hi:[1,0]
	v_pk_mul_f32 v[28:29], v[66:67], v[20:21] op_sel_hi:[1,0]
	v_add_f32_e32 v24, 1.0, v24
	v_add_f32_e32 v25, 1.0, v25
	v_rcp_f32_e32 v24, v24
	v_rcp_f32_e32 v25, v25
	s_nop 0
	v_pk_mul_f32 v[22:23], v[24:25], v[22:23]
	s_nop 0
	v_pk_mul_f32 v[22:23], v[22:23], v[26:27]
	v_lshlrev_b32_e32 v24, 16, v129
	v_cvt_pk_bf16_f32 v22, v22, v23
	v_mul_f32_e32 v23, 0xbfb8aa3b, v24
	v_exp_f32_e32 v23, v23
	v_and_b32_e32 v25, 0xffff0000, v129
	v_add_f32_e32 v23, 1.0, v23
	v_rcp_f32_e32 v26, v23
	v_mul_f32_e32 v23, 0xbfb8aa3b, v25
	v_exp_f32_e32 v23, v23
	s_nop 0
	v_add_f32_e32 v23, 1.0, v23
	v_rcp_f32_e32 v27, v23
	s_nop 0
	v_pk_mul_f32 v[24:25], v[26:27], v[24:25]
	s_nop 0
	v_pk_mul_f32 v[24:25], v[24:25], v[28:29]
	v_pk_mul_f32 v[26:27], v[60:61], v[20:21] op_sel_hi:[1,0]
	v_cvt_pk_bf16_f32 v23, v24, v25
	global_store_dwordx2 v[116:117], v[22:23], off
	v_lshlrev_b32_e32 v22, 16, v124
	v_and_b32_e32 v23, 0xffff0000, v124
	v_mul_f32_e32 v24, 0xbfb8aa3b, v22
	v_mul_f32_e32 v25, 0xbfb8aa3b, v23
	v_exp_f32_e32 v24, v24
	v_exp_f32_e32 v25, v25
	v_pk_mul_f32 v[28:29], v[62:63], v[20:21] op_sel_hi:[1,0]
	v_add_f32_e32 v24, 1.0, v24
	v_add_f32_e32 v25, 1.0, v25
	v_rcp_f32_e32 v24, v24
	v_rcp_f32_e32 v25, v25
	s_nop 0
	v_pk_mul_f32 v[22:23], v[24:25], v[22:23]
	s_nop 0
	v_pk_mul_f32 v[22:23], v[22:23], v[26:27]
	v_lshlrev_b32_e32 v24, 16, v125
	v_cvt_pk_bf16_f32 v22, v22, v23
	v_mul_f32_e32 v23, 0xbfb8aa3b, v24
	v_exp_f32_e32 v23, v23
	v_and_b32_e32 v25, 0xffff0000, v125
	v_add_f32_e32 v23, 1.0, v23
	v_rcp_f32_e32 v26, v23
	v_mul_f32_e32 v23, 0xbfb8aa3b, v25
	v_exp_f32_e32 v23, v23
	s_nop 0
	v_add_f32_e32 v23, 1.0, v23
	v_rcp_f32_e32 v27, v23
	s_nop 0
	v_pk_mul_f32 v[24:25], v[26:27], v[24:25]
	s_nop 0
	v_pk_mul_f32 v[24:25], v[24:25], v[28:29]
	v_pk_mul_f32 v[26:27], v[56:57], v[20:21] op_sel_hi:[1,0]
	v_cvt_pk_bf16_f32 v23, v24, v25
	global_store_dwordx2 v[116:117], v[22:23], off offset:32
	v_lshlrev_b32_e32 v22, 16, v122
	v_and_b32_e32 v23, 0xffff0000, v122
	v_mul_f32_e32 v24, 0xbfb8aa3b, v22
	v_mul_f32_e32 v25, 0xbfb8aa3b, v23
	v_exp_f32_e32 v24, v24
	v_exp_f32_e32 v25, v25
	v_add_f32_e32 v24, 1.0, v24
	v_add_f32_e32 v25, 1.0, v25
	v_rcp_f32_e32 v24, v24
	v_rcp_f32_e32 v25, v25
	s_nop 0
	v_pk_mul_f32 v[22:23], v[24:25], v[22:23]
	s_nop 0
	v_pk_mul_f32 v[22:23], v[22:23], v[26:27]
	v_lshlrev_b32_e32 v24, 16, v123
	v_cvt_pk_bf16_f32 v22, v22, v23
	v_mul_f32_e32 v23, 0xbfb8aa3b, v24
	v_exp_f32_e32 v23, v23
	v_and_b32_e32 v25, 0xffff0000, v123
	v_pk_mul_f32 v[26:27], v[58:59], v[20:21] op_sel_hi:[1,0]
	v_add_f32_e32 v23, 1.0, v23
	v_rcp_f32_e32 v28, v23
	v_mul_f32_e32 v23, 0xbfb8aa3b, v25
	v_exp_f32_e32 v23, v23
	s_nop 0
	v_add_f32_e32 v23, 1.0, v23
	v_rcp_f32_e32 v29, v23
	s_nop 0
	v_pk_mul_f32 v[24:25], v[28:29], v[24:25]
	s_nop 0
	v_pk_mul_f32 v[24:25], v[24:25], v[26:27]
	v_pk_mul_f32 v[26:27], v[52:53], v[20:21] op_sel_hi:[1,0]
	v_cvt_pk_bf16_f32 v23, v24, v25
	global_store_dwordx2 v[116:117], v[22:23], off offset:64
	v_lshlrev_b32_e32 v22, 16, v118
	v_and_b32_e32 v23, 0xffff0000, v118
	v_mul_f32_e32 v24, 0xbfb8aa3b, v22
	v_mul_f32_e32 v25, 0xbfb8aa3b, v23
	v_exp_f32_e32 v24, v24
	v_exp_f32_e32 v25, v25
	v_pk_mul_f32 v[28:29], v[54:55], v[20:21] op_sel_hi:[1,0]
	v_add_f32_e32 v24, 1.0, v24
	v_add_f32_e32 v25, 1.0, v25
	v_rcp_f32_e32 v24, v24
	v_rcp_f32_e32 v25, v25
	s_nop 0
	v_pk_mul_f32 v[22:23], v[24:25], v[22:23]
	s_nop 0
	v_pk_mul_f32 v[22:23], v[22:23], v[26:27]
	v_lshlrev_b32_e32 v24, 16, v119
	v_and_b32_e32 v25, 0xffff0000, v119
	v_cvt_pk_bf16_f32 v22, v22, v23
	v_mul_f32_e32 v23, 0xbfb8aa3b, v24
	v_mul_f32_e32 v20, 0xbfb8aa3b, v25
	v_exp_f32_e32 v23, v23
	v_exp_f32_e32 v20, v20
	v_add_f32_e32 v23, 1.0, v23
	v_add_f32_e32 v20, 1.0, v20
	v_rcp_f32_e32 v26, v23
	v_rcp_f32_e32 v27, v20
	v_mov_b32_e32 v20, v130
	v_mov_b32_e32 v238, v130
	s_nop 1
	v_permlane16_swap_b32 v20, v238
	v_pk_mul_f32 v[24:25], v[26:27], v[24:25]
	s_nop 0
	v_pk_mul_f32 v[24:25], v[24:25], v[28:29]
	s_waitcnt lgkmcnt(0)
; __device__ __forceinline__ float fexp2(float x) { return __builtin_amdgcn_exp2f(x); }
; __device__ __forceinline__ float siluf_(float x) { return x * __builtin_amdgcn_rcpf(1.f + fexp(-x)); }
; __device__ __forceinline__ float lo16(unsigned u) { return __uint_as_float(u << 16); }
; __device__ __forceinline__ float hi16(unsigned u) { return __uint_as_float(u & 0xffff0000u); }
; __device__ void phase_swa_mfma(const Params& p, int l, char* smem, int vb, int nvb, int pend, int oz) {
;     ...
;         for (int qt2 = 0; qt2 < 2; ++qt2) {
;             float ls = lsum[qt2];
;             ls += __shfl_xor(ls, 16);
;             ls += __shfl_xor(ls, 32);
;             const float mn = fmaxf(m[qt2], snk);
;             const float s1 = fexp2(m[qt2] - mn);
;             const float inv = s1 / (ls * s1 + fexp2(snk - mn));
;             const int tq = qt * 64 + 32 * qsub + 16 * qt2 + li;
;             bf16_t* zp = U + (qbase + tq) * LDU + C_SZ + hq * 64 + 4 * g;
; #pragma unroll
;             for (int dt = 0; dt < 4; ++dt) {
;                 const u32x2 zv = zpre[qt2][dt];
;                 u32x2 yv;
;                 yv[0] = cvt_pk(O[dt][qt2][0] * inv * siluf_(lo16(zv[0])), O[dt][qt2][1] * inv * siluf_(hi16(zv[0])));
;                 yv[1] = cvt_pk(O[dt][qt2][2] * inv * siluf_(lo16(zv[1])), O[dt][qt2][3] * inv * siluf_(hi16(zv[1])));
;                 *(u32x2*)(zp + 16 * dt) = yv;
;             }
	v_add_f32_e32 v20, v20, v238
	v_cvt_pk_bf16_f32 v23, v24, v25
	global_store_dwordx2 v[116:117], v[22:23], off offset:96
	v_mov_b32_e32 v22, v20
	v_mov_b32_e32 v238, v20
	s_nop 1
	v_permlane32_swap_b32 v22, v238
	v_and_b32_e32 v27, 0xffff0000, v114
	s_waitcnt lgkmcnt(0)
	v_add_f32_e32 v20, v22, v238
	v_max_f32_e32 v22, v105, v105
	v_max_f32_e32 v22, v22, v30
	v_sub_f32_e32 v23, v105, v22
	v_fma_f32 v21, v21, s4, -v22
	v_exp_f32_e32 v23, v23
	v_exp_f32_e32 v21, v21
	v_mov_b32_e32 v105, v3
	v_fmac_f32_e32 v21, v23, v20
	v_div_scale_f32 v20, s[2:3], v21, v21, v23
	v_rcp_f32_e32 v22, v20
	s_mov_b64 s[2:3], 0x1800
	v_fma_f32 v24, -v20, v22, 1.0
	v_fmac_f32_e32 v22, v24, v22
	v_div_scale_f32 v24, vcc, v23, v21, v23
	v_mul_f32_e32 v25, v24, v22
	v_fma_f32 v26, -v20, v25, v24
	v_fmac_f32_e32 v25, v26, v22
	v_fma_f32 v20, -v20, v25, v24
	v_div_fmas_f32 v20, v20, v22, v25
	v_lshlrev_b32_e32 v26, 16, v114
	v_div_fixup_f32 v22, v20, v21, v23
	v_mul_f32_e32 v23, 0xbfb8aa3b, v26
	v_exp_f32_e32 v23, v23
	v_lshl_add_u64 v[20:21], v[108:109], 0, s[20:21]
	v_lshl_add_u64 v[24:25], v[20:21], 0, v[104:105]
	v_lshl_add_u64 v[20:21], v[24:25], 0, s[2:3]
	v_add_f32_e32 v23, 1.0, v23
	v_rcp_f32_e32 v28, v23
	v_pk_mul_f32 v[12:13], v[12:13], v[22:23] op_sel_hi:[1,0]
	v_mul_f32_e32 v23, 0xbfb8aa3b, v27
	v_exp_f32_e32 v23, v23
	s_nop 0
	v_add_f32_e32 v23, 1.0, v23
	v_rcp_f32_e32 v29, v23
	v_pk_mul_f32 v[14:15], v[14:15], v[22:23] op_sel_hi:[1,0]
	v_pk_mul_f32 v[4:5], v[4:5], v[22:23] op_sel_hi:[1,0]
	v_pk_mul_f32 v[6:7], v[6:7], v[22:23] op_sel_hi:[1,0]
	v_pk_mul_f32 v[26:27], v[28:29], v[26:27]
	v_pk_mul_f32 v[8:9], v[8:9], v[22:23] op_sel_hi:[1,0]
	v_pk_mul_f32 v[12:13], v[26:27], v[12:13]
	v_lshlrev_b32_e32 v26, 16, v115
	v_cvt_pk_bf16_f32 v12, v12, v13
	v_mul_f32_e32 v13, 0xbfb8aa3b, v26
	v_exp_f32_e32 v13, v13
	v_and_b32_e32 v27, 0xffff0000, v115
	v_pk_mul_f32 v[10:11], v[10:11], v[22:23] op_sel_hi:[1,0]
	v_add_f32_e32 v13, 1.0, v13
	v_rcp_f32_e32 v28, v13
	v_mul_f32_e32 v13, 0xbfb8aa3b, v27
	v_exp_f32_e32 v13, v13
	s_nop 0
	v_add_f32_e32 v13, 1.0, v13
	v_rcp_f32_e32 v29, v13
	s_nop 0
	v_pk_mul_f32 v[26:27], v[28:29], v[26:27]
	s_nop 0
	v_pk_mul_f32 v[14:15], v[26:27], v[14:15]
	s_nop 0
	v_cvt_pk_bf16_f32 v13, v14, v15
	v_add_co_u32_e32 v14, vcc, s22, v24
	s_nop 1
	v_addc_co_u32_e32 v15, vcc, 0, v25, vcc
	global_store_dwordx2 v[14:15], v[12:13], off offset:2048
	v_lshlrev_b32_e32 v12, 16, v112
	v_and_b32_e32 v13, 0xffff0000, v112
	v_mul_f32_e32 v14, 0xbfb8aa3b, v12
	v_mul_f32_e32 v15, 0xbfb8aa3b, v13
	v_exp_f32_e32 v14, v14
	v_exp_f32_e32 v15, v15
	v_add_f32_e32 v14, 1.0, v14
	v_add_f32_e32 v15, 1.0, v15
	v_rcp_f32_e32 v14, v14
	v_rcp_f32_e32 v15, v15
	s_nop 0
	v_pk_mul_f32 v[12:13], v[14:15], v[12:13]
	s_nop 0
	v_pk_mul_f32 v[4:5], v[12:13], v[4:5]
	v_lshlrev_b32_e32 v12, 16, v113
	v_cvt_pk_bf16_f32 v4, v4, v5
	v_mul_f32_e32 v5, 0xbfb8aa3b, v12
	v_exp_f32_e32 v5, v5
	v_and_b32_e32 v13, 0xffff0000, v113
	v_add_f32_e32 v5, 1.0, v5
	v_rcp_f32_e32 v14, v5
	v_mul_f32_e32 v5, 0xbfb8aa3b, v13
	v_exp_f32_e32 v5, v5
	s_nop 0
	v_add_f32_e32 v5, 1.0, v5
	v_rcp_f32_e32 v15, v5
	s_nop 0
	v_pk_mul_f32 v[12:13], v[14:15], v[12:13]
	s_nop 0
	v_pk_mul_f32 v[6:7], v[12:13], v[6:7]
	s_nop 0
	v_cvt_pk_bf16_f32 v5, v6, v7
	global_store_dwordx2 v[20:21], v[4:5], off offset:32
	v_lshlrev_b32_e32 v4, 16, v110
	v_and_b32_e32 v5, 0xffff0000, v110
	v_mul_f32_e32 v6, 0xbfb8aa3b, v4
	v_mul_f32_e32 v7, 0xbfb8aa3b, v5
	v_exp_f32_e32 v6, v6
	v_exp_f32_e32 v7, v7
	v_add_f32_e32 v6, 1.0, v6
	v_add_f32_e32 v7, 1.0, v7
	v_rcp_f32_e32 v6, v6
	v_rcp_f32_e32 v7, v7
	s_nop 0
	v_pk_mul_f32 v[4:5], v[6:7], v[4:5]
	s_nop 0
	v_pk_mul_f32 v[4:5], v[4:5], v[8:9]
	v_lshlrev_b32_e32 v6, 16, v111
	v_cvt_pk_bf16_f32 v4, v4, v5
	v_mul_f32_e32 v5, 0xbfb8aa3b, v6
	v_exp_f32_e32 v5, v5
	v_and_b32_e32 v7, 0xffff0000, v111
	v_add_f32_e32 v5, 1.0, v5
	v_rcp_f32_e32 v8, v5
	v_mul_f32_e32 v5, 0xbfb8aa3b, v7
	v_exp_f32_e32 v5, v5
	s_nop 0
	v_add_f32_e32 v5, 1.0, v5
	v_rcp_f32_e32 v9, v5
	s_nop 0
	v_pk_mul_f32 v[6:7], v[8:9], v[6:7]
	s_nop 0
	v_pk_mul_f32 v[6:7], v[6:7], v[10:11]
	v_pk_mul_f32 v[8:9], v[16:17], v[22:23] op_sel_hi:[1,0]
	v_cvt_pk_bf16_f32 v5, v6, v7
	global_store_dwordx2 v[20:21], v[4:5], off offset:64
	v_lshlrev_b32_e32 v4, 16, v106
	v_and_b32_e32 v5, 0xffff0000, v106
	v_mul_f32_e32 v6, 0xbfb8aa3b, v4
	v_mul_f32_e32 v7, 0xbfb8aa3b, v5
	v_exp_f32_e32 v6, v6
	v_exp_f32_e32 v7, v7
	v_pk_mul_f32 v[10:11], v[18:19], v[22:23] op_sel_hi:[1,0]
	v_add_f32_e32 v6, 1.0, v6
	v_add_f32_e32 v7, 1.0, v7
	v_rcp_f32_e32 v6, v6
	v_rcp_f32_e32 v7, v7
	s_nop 0
	v_pk_mul_f32 v[4:5], v[6:7], v[4:5]
	s_nop 0
	v_pk_mul_f32 v[4:5], v[4:5], v[8:9]
	v_lshlrev_b32_e32 v6, 16, v107
	v_cvt_pk_bf16_f32 v4, v4, v5
	v_mul_f32_e32 v5, 0xbfb8aa3b, v6
	v_exp_f32_e32 v5, v5
	v_and_b32_e32 v7, 0xffff0000, v107
	v_add_f32_e32 v5, 1.0, v5
	v_rcp_f32_e32 v8, v5
	v_mul_f32_e32 v5, 0xbfb8aa3b, v7
	v_exp_f32_e32 v5, v5
	s_nop 0
	v_add_f32_e32 v5, 1.0, v5
	v_rcp_f32_e32 v9, v5
	s_nop 0
	v_pk_mul_f32 v[6:7], v[8:9], v[6:7]
	s_nop 0
	v_pk_mul_f32 v[6:7], v[6:7], v[10:11]
	s_nop 0
	v_cvt_pk_bf16_f32 v5, v6, v7
	global_store_dwordx2 v[20:21], v[4:5], off offset:96
	s_cbranch_scc1 .LBB0_232

; __device__ __forceinline__ float lo16(unsigned u) { return __uint_as_float(u << 16); }
; __device__ __forceinline__ float hi16(unsigned u) { return __uint_as_float(u & 0xffff0000u); }
; __device__ void phase_swa_mfma(const Params& p, int l, char* smem, int vb, int nvb, int pend, int oz) {
;     ...
;         for (int qt2 = 0; qt2 < 2; ++qt2) {
;             const int tq = qt * 64 + 32 * qsub + 16 * qt2 + li;
;             const bf16_t* qp = U + (qbase + tq) * LDU + C_SQ + hq * 64 + 8 * g;
;             const u32x4 r0 = *(const u32x4*)qp, r1 = *(const u32x4*)(qp + 32);
;             float x1[8], x2[8];
; #pragma unroll
;             for (int w = 0; w < 4; ++w) {
;                 x1[2 * w] = lo16(r0[w]); x1[2 * w + 1] = hi16(r0[w]);
;                 x2[2 * w] = lo16(r1[w]); x2[2 * w + 1] = hi16(r1[w]);
;             }
;             if (!cq) {
;                 const float pos = (g < 2) ? (float)(tq >> 6) : (float)(tq & 63);
; #pragma unroll
;                 for (int j = 0; j < 8; ++j) {
;                     float rev = pos * invq[j];
;                     rev -= floorf(rev);
;                     const float cs = __builtin_amdgcn_cosf(rev), sn = __builtin_amdgcn_sinf(rev);
;                     const float a1 = x1[j], a2 = x2[j];
;                     x1[j] = a1 * cs - a2 * sn;
;                     x2[j] = a1 * sn + a2 * cs;
;                 }
;             }
;     ...
;         u32x2 zpre[2][4];
; #pragma unroll
;         for (int qt2 = 0; qt2 < 2; ++qt2)
; #pragma unroll
;             for (int dt = 0; dt < 4; ++dt)
;                 zpre[qt2][dt] = *(const u32x2*)(U + (qbase + qt * 64 + 32 * qsub + 16 * qt2 + li) * LDU + C_SZ + hq * 64 + 4 * g + 16 * dt);
;         float m[2] = {-1e30f, -1e30f}, lsum[2] = {0.f, 0.f};
;         f32x4 O[4][2];
; #pragma unroll
;         for (int dt = 0; dt < 4; ++dt)
; #pragma unroll
;             for (int qt2 = 0; qt2 < 2; ++qt2) O[dt][qt2] = (f32x4){0.f, 0.f, 0.f, 0.f};
;         const int nloc = cq ? 0 : 5;
;         u32x4 pk0, pk1, pv0, pv1;
;     ...
;         SWA_PREFETCH(0)
.LBB0_183:
	s_and_b32 s2, s21, 1
	s_lshl_b32 s80, s2, 1
	s_ashr_i32 s21, s20, 31
	s_add_i32 s80, s80, s55
	s_lshl_b64 s[50:51], s[20:21], 8
	s_add_u32 s44, s50, 0x4000
	s_addc_u32 s45, s51, 0
	s_lshl_b64 s[46:47], s[20:21], 11
	s_and_b64 s[20:21], s[40:41], exec
	s_cselect_b32 s21, s47, s45
	s_cselect_b32 s20, s46, s44
	v_or_b32_e32 v120, s24, v166
	v_mov_b32_e32 v121, v3
	v_lshl_add_u64 v[6:7], s[20:21], 0, v[120:121]
	v_mov_b64_e32 v[4:5], s[34:35]
	v_mad_u64_u32 v[4:5], s[24:25], v6, s92, v[4:5]
	v_mad_i32_i24 v5, v7, s92, v5
	s_lshl_b32 s96, s80, 7
	v_lshl_add_u64 v[8:9], v[4:5], 0, s[96:97]
	v_lshlrev_b32_e32 v6, 1, v100
	v_mov_b32_e32 v7, v3
	v_lshl_add_u64 v[12:13], v[8:9], 0, v[6:7]
	v_add_co_u32_e32 v8, vcc, s22, v12
	s_mov_b64 s[4:5], 0x1400
	s_nop 0
	v_addc_co_u32_e32 v9, vcc, 0, v13, vcc
	v_lshl_add_u64 v[12:13], v[12:13], 0, s[4:5]
	s_mov_b64 s[4:5], 0x1a800
	v_lshl_add_u64 v[238:239], v[8:9], 0, s[4:5]
	v_lshl_add_u64 v[240:241], v[12:13], 0, s[4:5]
	s_mov_b64 s[4:5], 0x1400
	global_load_dwordx4 v[8:11], v[8:9], off offset:1024
	v_cndmask_b32_e64 v7, 0, 1, s[40:41]
	global_load_dwordx4 v[12:15], v[12:13], off offset:64
	global_load_dwordx4 v[226:229], v[238:239], off offset:1024
	global_load_dwordx4 v[230:233], v[240:241], off offset:64
	v_or_b32_e32 v176, s3, v160
	v_or_b32_e32 v177, 0x4000, v176
	v_cndmask_b32_e64 v176, v177, v176, s[40:41]
	v_mov_b32_e32 v177, v3
	s_and_b64 s[4:5], s[40:41], exec
	s_cselect_b32 s5, s47, s51
	s_cselect_b32 s4, s46, s50
	v_lshl_add_u64 v[176:177], s[4:5], 0, v[176:177]
	v_mov_b64_e32 v[178:179], s[34:35]
	v_mad_u64_u32 v[178:179], vcc, v176, s92, v[178:179]
	v_mad_i32_i24 v179, v177, s92, v179
	s_lshl_b32 s4, s2, 7
	s_mov_b32 s5, 0
	v_lshl_add_u64 v[176:177], v[178:179], 0, s[4:5]
	v_lshl_add_u64 v[176:177], v[176:177], 0, v[2:3]
	s_mov_b64 s[4:5], 0x1600
	v_lshl_add_u64 v[178:179], v[176:177], 0, s[4:5]
	s_mov_b64 s[4:5], 0x1700
	v_lshl_add_u64 v[180:181], v[176:177], 0, s[4:5]
	s_mov_b64 s[4:5], 0x1000
	v_lshl_add_u64 v[176:177], v[176:177], 0, s[4:5]
	global_load_dwordx4 v[184:187], v[176:177], off offset:1536
	global_load_dwordx4 v[188:191], v[176:177], off offset:1792
	global_load_dwordx4 v[192:195], v[178:179], off offset:64
	global_load_dwordx4 v[200:203], v[180:181], off offset:64
	s_lshl_b32 s4, s80, 7
	s_mov_b32 s5, 0
	v_lshl_add_u64 v[176:177], v[4:5], 0, s[4:5]
	v_mov_b32_e32 v182, v104
	v_mov_b32_e32 v183, v3
	v_lshl_add_u64 v[176:177], v[176:177], 0, v[182:183]
	s_mov_b32 s4, s22
	v_lshl_add_u64 v[178:179], v[176:177], 0, s[4:5]
	s_mov_b64 s[4:5], 0x1800
	v_lshl_add_u64 v[180:181], v[176:177], 0, s[4:5]
	global_load_dwordx2 v[204:205], v[178:179], off offset:2048
	global_load_dwordx2 v[206:207], v[180:181], off offset:32
	global_load_dwordx2 v[208:209], v[180:181], off offset:64
	global_load_dwordx2 v[210:211], v[180:181], off offset:96
	s_mov_b64 s[4:5], 0x1c000
	v_lshl_add_u64 v[178:179], v[176:177], 0, s[4:5]
	global_load_dwordx2 v[212:213], v[178:179], off
	global_load_dwordx2 v[214:215], v[178:179], off offset:32
	global_load_dwordx2 v[216:217], v[178:179], off offset:64
	global_load_dwordx2 v[218:219], v[178:179], off offset:96
	s_mov_b64 s[4:5], 0x1400
	v_cmp_ne_u32_e64 s[42:43], 1, v7
	s_andn2_b64 vcc, exec, s[40:41]
	s_waitcnt vmcnt(14)
	v_and_b32_e32 v28, 0xffff0000, v8
	v_lshlrev_b32_e32 v29, 16, v8
	v_and_b32_e32 v32, 0xffff0000, v12
	v_lshlrev_b32_e32 v33, 16, v12
	v_and_b32_e32 v42, 0xffff0000, v9
	v_lshlrev_b32_e32 v43, 16, v9
	v_and_b32_e32 v30, 0xffff0000, v13
	v_lshlrev_b32_e32 v31, 16, v13
	v_and_b32_e32 v40, 0xffff0000, v10
	v_lshlrev_b32_e32 v41, 16, v10
	v_and_b32_e32 v34, 0xffff0000, v14
	v_lshlrev_b32_e32 v35, 16, v14
	v_and_b32_e32 v38, 0xffff0000, v11
	v_lshlrev_b32_e32 v39, 16, v11
	v_and_b32_e32 v36, 0xffff0000, v15
	v_lshlrev_b32_e32 v37, 16, v15
	s_cbranch_vccnz .LBB0_185
	v_and_b32_e32 v7, 47, v120
	v_mov_b32_e32 v8, s57
	v_cndmask_b32_e64 v7, v7, v8, s[36:37]
	v_cvt_f32_u32_e32 v7, v7
	v_mul_f32_e32 v8, v1, v7
	v_floor_f32_e32 v8, v8
	v_fma_f32 v8, v1, v7, -v8
	v_cos_f32_e32 v9, v8
	v_sin_f32_e32 v11, v8
	v_mul_f32_e32 v8, v103, v7
	v_floor_f32_e32 v8, v8
	v_fma_f32 v10, v103, v7, -v8
	v_cos_f32_e32 v8, v10
	v_sin_f32_e32 v10, v10
	s_nop 0
	v_pk_mul_f32 v[12:13], v[10:11], v[32:33]
	s_nop 0
	v_pk_fma_f32 v[12:13], v[8:9], v[28:29], v[12:13] neg_lo:[0,0,1] neg_hi:[0,0,1]
	v_pk_mul_f32 v[8:9], v[8:9], v[32:33]
	s_nop 0
	v_pk_fma_f32 v[32:33], v[10:11], v[28:29], v[8:9]
	v_mul_f32_e32 v8, v148, v7
	v_floor_f32_e32 v8, v8
	v_fma_f32 v8, v148, v7, -v8
	v_cos_f32_e32 v9, v8
	v_sin_f32_e32 v11, v8
	v_mul_f32_e32 v8, v150, v7
	v_floor_f32_e32 v8, v8
	v_fma_f32 v10, v150, v7, -v8
	v_cos_f32_e32 v8, v10
	v_sin_f32_e32 v10, v10
	v_mov_b64_e32 v[28:29], v[12:13]
	v_pk_mul_f32 v[14:15], v[10:11], v[30:31]
	s_nop 0
	v_pk_fma_f32 v[14:15], v[8:9], v[42:43], v[14:15] neg_lo:[0,0,1] neg_hi:[0,0,1]
	v_pk_mul_f32 v[8:9], v[8:9], v[30:31]
	s_nop 0
	v_pk_fma_f32 v[30:31], v[10:11], v[42:43], v[8:9]
	v_mul_f32_e32 v8, v152, v7
	v_floor_f32_e32 v8, v8
	v_fma_f32 v8, v152, v7, -v8
	v_cos_f32_e32 v9, v8
	v_sin_f32_e32 v11, v8
	v_mul_f32_e32 v8, v154, v7
	v_floor_f32_e32 v8, v8
	v_fma_f32 v10, v154, v7, -v8
	v_cos_f32_e32 v8, v10
	v_sin_f32_e32 v10, v10
	v_mov_b64_e32 v[42:43], v[14:15]
	v_pk_mul_f32 v[16:17], v[10:11], v[34:35]
	s_nop 0
	v_pk_fma_f32 v[16:17], v[8:9], v[40:41], v[16:17] neg_lo:[0,0,1] neg_hi:[0,0,1]
	v_pk_mul_f32 v[8:9], v[8:9], v[34:35]
	s_nop 0
	v_pk_fma_f32 v[34:35], v[10:11], v[40:41], v[8:9]
	v_mul_f32_e32 v8, v156, v7
	v_floor_f32_e32 v8, v8
	v_fma_f32 v8, v156, v7, -v8
	v_cos_f32_e32 v9, v8
	v_sin_f32_e32 v11, v8
	v_mul_f32_e32 v8, v158, v7
	v_floor_f32_e32 v8, v8
	v_fma_f32 v7, v158, v7, -v8
	v_sin_f32_e32 v10, v7
	v_cos_f32_e32 v8, v7
	v_mov_b64_e32 v[40:41], v[16:17]
	v_pk_mul_f32 v[18:19], v[10:11], v[36:37]
	s_nop 0
	v_pk_fma_f32 v[18:19], v[8:9], v[38:39], v[18:19] neg_lo:[0,0,1] neg_hi:[0,0,1]
	v_pk_mul_f32 v[8:9], v[8:9], v[36:37]
	s_nop 0
	v_pk_fma_f32 v[36:37], v[10:11], v[38:39], v[8:9]
	v_mov_b64_e32 v[38:39], v[18:19]
; __device__ __forceinline__ float lo16(unsigned u) { return __uint_as_float(u << 16); }
; __device__ __forceinline__ float hi16(unsigned u) { return __uint_as_float(u & 0xffff0000u); }
; __device__ void phase_swa_mfma(const Params& p, int l, char* smem, int vb, int nvb, int pend, int oz) {
;     ...
;         for (int qt2 = 0; qt2 < 2; ++qt2) {
;             const int tq = qt * 64 + 32 * qsub + 16 * qt2 + li;
;             const bf16_t* qp = U + (qbase + tq) * LDU + C_SQ + hq * 64 + 8 * g;
;             const u32x4 r0 = *(const u32x4*)qp, r1 = *(const u32x4*)(qp + 32);
;             float x1[8], x2[8];
; #pragma unroll
;             for (int w = 0; w < 4; ++w) {
;                 x1[2 * w] = lo16(r0[w]); x1[2 * w + 1] = hi16(r0[w]);
;                 x2[2 * w] = lo16(r1[w]); x2[2 * w + 1] = hi16(r1[w]);
;             }
;             if (!cq) {
;                 const float pos = (g < 2) ? (float)(tq >> 6) : (float)(tq & 63);
; #pragma unroll
;                 for (int j = 0; j < 8; ++j) {
;                     float rev = pos * invq[j];
;                     rev -= floorf(rev);
;                     const float cs = __builtin_amdgcn_cosf(rev), sn = __builtin_amdgcn_sinf(rev);
;                     const float a1 = x1[j], a2 = x2[j];
;                     x1[j] = a1 * cs - a2 * sn;
;                     x2[j] = a1 * sn + a2 * cs;
;                 }
;             }
;             u32x4 o1, o2;
; #pragma unroll
;             for (int w = 0; w < 4; ++w) {
;                 o1[w] = cvt_pk(x1[2 * w] * QSC, x1[2 * w + 1] * QSC);
;                 o2[w] = cvt_pk(x2[2 * w] * QSC, x2[2 * w + 1] * QSC);
;             }
;             qf[qt2][0] = __builtin_bit_cast(bf16x8, o1);
;             qf[qt2][1] = __builtin_bit_cast(bf16x8, o2);
;     ...
;         u32x2 zpre[2][4];
; #pragma unroll
;         for (int qt2 = 0; qt2 < 2; ++qt2)
; #pragma unroll
;             for (int dt = 0; dt < 4; ++dt)
;                 zpre[qt2][dt] = *(const u32x2*)(U + (qbase + qt * 64 + 32 * qsub + 16 * qt2 + li) * LDU + C_SZ + hq * 64 + 4 * g + 16 * dt);
;         float m[2] = {-1e30f, -1e30f}, lsum[2] = {0.f, 0.f};
;         f32x4 O[4][2];
; #pragma unroll
;         for (int dt = 0; dt < 4; ++dt)
; #pragma unroll
;             for (int qt2 = 0; qt2 < 2; ++qt2) O[dt][qt2] = (f32x4){0.f, 0.f, 0.f, 0.f};
;         const int nloc = cq ? 0 : 5;
;         u32x4 pk0, pk1, pv0, pv1;
;     ...
;         SWA_PREFETCH(0)
.LBB0_185:
	v_or_b32_e32 v126, 16, v120
	v_mov_b32_e32 v127, v3
	v_lshl_add_u64 v[8:9], s[20:21], 0, v[126:127]
	v_mov_b64_e32 v[10:11], s[34:35]
	v_mad_u64_u32 v[108:109], s[20:21], v8, s92, v[10:11]
	v_mov_b32_e32 v8, v109
	s_lshl_b32 s24, s80, 6
	v_mad_u64_u32 v[8:9], s[20:21], v9, s92, v[8:9]
	v_mov_b32_e32 v109, v8
	s_lshl_b32 s20, s24, 1
	s_mov_b32 s21, s97
	v_lshl_add_u64 v[8:9], v[108:109], 0, s[20:21]
	v_mov_b32_e32 v7, v3
	v_lshl_add_u64 v[10:11], v[8:9], 0, v[6:7]
	v_add_co_u32_e32 v6, vcc, s22, v10
	s_mov_b32 s81, 0
	s_nop 0
	v_addc_co_u32_e32 v7, vcc, 0, v11, vcc
	v_lshl_add_u64 v[10:11], v[10:11], 0, s[4:5]
	s_and_b64 vcc, exec, s[42:43]
	s_waitcnt vmcnt(12)
	v_mov_b64_e32 v[6:7], v[226:227]
	v_mov_b64_e32 v[8:9], v[228:229]
	v_mov_b64_e32 v[10:11], v[230:231]
	v_mov_b64_e32 v[12:13], v[232:233]
	v_and_b32_e32 v20, 0xffff0000, v6
	v_lshlrev_b32_e32 v21, 16, v6
	v_and_b32_e32 v24, 0xffff0000, v10
	v_lshlrev_b32_e32 v25, 16, v10
	v_and_b32_e32 v50, 0xffff0000, v7
	v_lshlrev_b32_e32 v51, 16, v7
	v_and_b32_e32 v22, 0xffff0000, v11
	v_lshlrev_b32_e32 v23, 16, v11
	v_and_b32_e32 v48, 0xffff0000, v8
	v_lshlrev_b32_e32 v49, 16, v8
	v_and_b32_e32 v26, 0xffff0000, v12
	v_lshlrev_b32_e32 v27, 16, v12
	v_and_b32_e32 v46, 0xffff0000, v9
	v_lshlrev_b32_e32 v47, 16, v9
	v_and_b32_e32 v44, 0xffff0000, v13
	v_lshlrev_b32_e32 v45, 16, v13
	s_cbranch_vccnz .LBB0_187
	v_and_b32_e32 v6, 63, v126
	v_mov_b32_e32 v7, s57
	v_cndmask_b32_e64 v6, v6, v7, s[36:37]
	v_cvt_f32_u32_e32 v16, v6
	s_mov_b32 s81, 5
	s_mov_b64 s[50:51], s[46:47]
	v_mul_f32_e32 v6, v1, v16
	v_floor_f32_e32 v6, v6
	v_fma_f32 v6, v1, v16, -v6
	v_cos_f32_e32 v7, v6
	v_sin_f32_e32 v9, v6
	v_mul_f32_e32 v6, v103, v16
	v_floor_f32_e32 v6, v6
	v_fma_f32 v8, v103, v16, -v6
	v_cos_f32_e32 v6, v8
	v_sin_f32_e32 v8, v8
	s_nop 0
	v_pk_mul_f32 v[10:11], v[8:9], v[24:25]
	s_nop 0
	v_pk_fma_f32 v[10:11], v[6:7], v[20:21], v[10:11] neg_lo:[0,0,1] neg_hi:[0,0,1]
	v_pk_mul_f32 v[6:7], v[6:7], v[24:25]
	s_nop 0
	v_pk_fma_f32 v[24:25], v[8:9], v[20:21], v[6:7]
	v_mul_f32_e32 v6, v148, v16
	v_floor_f32_e32 v6, v6
	v_fma_f32 v6, v148, v16, -v6
	v_cos_f32_e32 v7, v6
	v_sin_f32_e32 v9, v6
	v_mul_f32_e32 v6, v150, v16
	v_floor_f32_e32 v6, v6
	v_fma_f32 v8, v150, v16, -v6
	v_cos_f32_e32 v6, v8
	v_sin_f32_e32 v8, v8
	v_mov_b64_e32 v[20:21], v[10:11]
	v_pk_mul_f32 v[12:13], v[8:9], v[22:23]
	s_nop 0
	v_pk_fma_f32 v[12:13], v[6:7], v[50:51], v[12:13] neg_lo:[0,0,1] neg_hi:[0,0,1]
	v_pk_mul_f32 v[6:7], v[6:7], v[22:23]
	s_nop 0
	v_pk_fma_f32 v[22:23], v[8:9], v[50:51], v[6:7]
	v_mul_f32_e32 v6, v152, v16
	v_floor_f32_e32 v6, v6
	v_fma_f32 v6, v152, v16, -v6
	v_cos_f32_e32 v7, v6
	v_sin_f32_e32 v9, v6
	v_mul_f32_e32 v6, v154, v16
	v_floor_f32_e32 v6, v6
	v_fma_f32 v8, v154, v16, -v6
	v_cos_f32_e32 v6, v8
	v_sin_f32_e32 v8, v8
	v_mov_b64_e32 v[50:51], v[12:13]
	v_pk_mul_f32 v[14:15], v[8:9], v[26:27]
	s_nop 0
	v_pk_fma_f32 v[14:15], v[6:7], v[48:49], v[14:15] neg_lo:[0,0,1] neg_hi:[0,0,1]
	v_pk_mul_f32 v[6:7], v[6:7], v[26:27]
	s_nop 0
	v_pk_fma_f32 v[26:27], v[8:9], v[48:49], v[6:7]
	v_mul_f32_e32 v6, v156, v16
	v_floor_f32_e32 v6, v6
	v_fma_f32 v6, v156, v16, -v6
	v_cos_f32_e32 v7, v6
	v_sin_f32_e32 v9, v6
	v_mul_f32_e32 v6, v158, v16
	v_floor_f32_e32 v6, v6
	v_fma_f32 v8, v158, v16, -v6
	v_cos_f32_e32 v6, v8
	v_sin_f32_e32 v8, v8
	v_mov_b64_e32 v[48:49], v[14:15]
	v_pk_mul_f32 v[16:17], v[8:9], v[44:45]
	s_nop 0
	v_pk_fma_f32 v[16:17], v[6:7], v[46:47], v[16:17] neg_lo:[0,0,1] neg_hi:[0,0,1]
	v_pk_mul_f32 v[6:7], v[6:7], v[44:45]
	s_nop 0
	v_pk_fma_f32 v[44:45], v[8:9], v[46:47], v[6:7]
	v_mov_b64_e32 v[46:47], v[16:17]
.LBB0_187:
	s_mov_b32 s21, s97
	v_mov_b32_e32 v105, v3
	v_lshl_add_u64 v[4:5], v[4:5], 0, s[20:21]
	v_lshl_add_u64 v[4:5], v[4:5], 0, v[104:105]
	v_add_co_u32_e32 v6, vcc, s22, v4
	s_mov_b64 s[4:5], 0x1800
	s_nop 0
	v_addc_co_u32_e32 v7, vcc, 0, v5, vcc
	s_mov_b64 s[24:25], 0x1c000
	s_mov_b32 s21, 0x1c000
	v_lshl_add_u64 v[116:117], v[4:5], 0, s[4:5]
	s_waitcnt vmcnt(0)
	v_mov_b64_e32 v[128:129], v[204:205]
	v_mov_b64_e32 v[124:125], v[206:207]
	v_mov_b64_e32 v[122:123], v[208:209]
	v_mov_b64_e32 v[118:119], v[210:211]
	v_lshl_add_u64 v[6:7], v[4:5], 0, s[24:25]
	v_add_co_u32_e32 v4, vcc, s21, v4
	s_lshl_b32 s96, s2, 7
	s_nop 0
	v_addc_co_u32_e32 v5, vcc, 0, v5, vcc
	v_mov_b64_e32 v[114:115], v[212:213]
	v_mov_b64_e32 v[112:113], v[214:215]
	v_mov_b64_e32 v[110:111], v[216:217]
	v_mov_b64_e32 v[106:107], v[218:219]
	v_or_b32_e32 v4, s3, v160
	v_or_b32_e32 v5, 0x4000, v4
	v_cndmask_b32_e64 v4, v5, v4, s[40:41]
	v_mov_b32_e32 v5, v3
	v_lshl_add_u64 v[4:5], s[50:51], 0, v[4:5]
	v_mov_b64_e32 v[6:7], s[34:35]
	v_mad_u64_u32 v[6:7], s[24:25], v4, s92, v[6:7]
	v_mad_i32_i24 v7, v5, s92, v7
	v_lshl_add_u64 v[4:5], v[6:7], 0, s[96:97]
	v_lshl_add_u64 v[4:5], v[4:5], 0, v[2:3]
	s_mov_b64 s[4:5], 0x1600
	v_lshl_add_u64 v[8:9], v[4:5], 0, s[4:5]
	s_mov_b64 s[4:5], 0x1700
	v_lshl_add_u64 v[10:11], v[4:5], 0, s[4:5]
	v_add_co_u32_e32 v4, vcc, 0x1000, v4
	s_mov_b64 s[42:43], -1
	s_nop 0
	v_addc_co_u32_e32 v5, vcc, 0, v5, vcc
	v_mov_b64_e32 v[16:17], v[184:185]
	v_mov_b64_e32 v[18:19], v[186:187]
	v_mov_b64_e32 v[4:5], v[188:189]
	v_mov_b64_e32 v[6:7], v[190:191]
	v_mov_b64_e32 v[12:13], v[192:193]
	v_mov_b64_e32 v[14:15], v[194:195]
	v_mov_b64_e32 v[8:9], v[200:201]
	v_mov_b64_e32 v[10:11], v[202:203]
	s_nop 0
	s_nop 0
	s_nop 0
	s_andn2_b64 vcc, exec, s[48:49]
	s_waitcnt lgkmcnt(0)
	s_barrier
	s_cbranch_vccnz .LBB0_189
	s_mov_b64 s[42:43], 0
